# final kernel: 16 dwordx4 partial loads per thread (16 row groups combined in LDS) instead of 64 dword loads
# speedup vs baseline: 1.0076x; 1.0076x over previous
_Z12final_kernelPKfPf:
	s_load_dwordx4 s[4:7], s[0:1], 0x0
	v_mul_u32_u24_e32 v1, 0x667, v0
	v_lshrrev_b32_e32 v1, 16, v1
	v_mul_u32_u24_e32 v2, 40, v1
	v_sub_u32_e32 v2, v0, v2
	s_mulk_i32 s2, 0xa0
	s_lshl_b32 s3, s2, 2
	v_mul_u32_u24_e32 v4, 0x28000, v1
	v_lshl_add_u32 v4, v2, 4, v4
	v_add_u32_e32 v4, s3, v4
	v_mul_u32_u24_e32 v5, 0x280, v1
	v_lshl_add_u32 v5, v2, 4, v5
	s_waitcnt lgkmcnt(0)
	s_mov_b64 s[8:9], s[4:5]
	global_load_dwordx4 v[14:17], v4, s[8:9]
	s_add_u32 s8, s8, 0x2800
	s_addc_u32 s9, s9, 0
	global_load_dwordx4 v[18:21], v4, s[8:9]
	s_add_u32 s8, s8, 0x2800
	s_addc_u32 s9, s9, 0
	global_load_dwordx4 v[22:25], v4, s[8:9]
	s_add_u32 s8, s8, 0x2800
	s_addc_u32 s9, s9, 0
	global_load_dwordx4 v[26:29], v4, s[8:9]
	s_add_u32 s8, s8, 0x2800
	s_addc_u32 s9, s9, 0
	global_load_dwordx4 v[30:33], v4, s[8:9]
	s_add_u32 s8, s8, 0x2800
	s_addc_u32 s9, s9, 0
	global_load_dwordx4 v[34:37], v4, s[8:9]
	s_add_u32 s8, s8, 0x2800
	s_addc_u32 s9, s9, 0
	global_load_dwordx4 v[38:41], v4, s[8:9]
	s_add_u32 s8, s8, 0x2800
	s_addc_u32 s9, s9, 0
	global_load_dwordx4 v[42:45], v4, s[8:9]
	s_add_u32 s8, s8, 0x2800
	s_addc_u32 s9, s9, 0
	global_load_dwordx4 v[46:49], v4, s[8:9]
	s_add_u32 s8, s8, 0x2800
	s_addc_u32 s9, s9, 0
	global_load_dwordx4 v[50:53], v4, s[8:9]
	s_add_u32 s8, s8, 0x2800
	s_addc_u32 s9, s9, 0
	global_load_dwordx4 v[54:57], v4, s[8:9]
	s_add_u32 s8, s8, 0x2800
	s_addc_u32 s9, s9, 0
	global_load_dwordx4 v[58:61], v4, s[8:9]
	s_add_u32 s8, s8, 0x2800
	s_addc_u32 s9, s9, 0
	global_load_dwordx4 v[62:65], v4, s[8:9]
	s_add_u32 s8, s8, 0x2800
	s_addc_u32 s9, s9, 0
	global_load_dwordx4 v[66:69], v4, s[8:9]
	s_add_u32 s8, s8, 0x2800
	s_addc_u32 s9, s9, 0
	global_load_dwordx4 v[70:73], v4, s[8:9]
	s_add_u32 s8, s8, 0x2800
	s_addc_u32 s9, s9, 0
	global_load_dwordx4 v[74:77], v4, s[8:9]
	v_mov_b32_e32 v10, 0
	v_mov_b32_e32 v11, 0
	v_mov_b32_e32 v12, 0
	v_mov_b32_e32 v13, 0
	s_waitcnt vmcnt(15)
	v_add_f32_e32 v10, v10, v14
	v_add_f32_e32 v11, v11, v15
	v_add_f32_e32 v12, v12, v16
	v_add_f32_e32 v13, v13, v17
	s_waitcnt vmcnt(14)
	v_add_f32_e32 v10, v10, v18
	v_add_f32_e32 v11, v11, v19
	v_add_f32_e32 v12, v12, v20
	v_add_f32_e32 v13, v13, v21
	s_waitcnt vmcnt(13)
	v_add_f32_e32 v10, v10, v22
	v_add_f32_e32 v11, v11, v23
	v_add_f32_e32 v12, v12, v24
	v_add_f32_e32 v13, v13, v25
	s_waitcnt vmcnt(12)
	v_add_f32_e32 v10, v10, v26
	v_add_f32_e32 v11, v11, v27
	v_add_f32_e32 v12, v12, v28
	v_add_f32_e32 v13, v13, v29
	s_waitcnt vmcnt(11)
	v_add_f32_e32 v10, v10, v30
	v_add_f32_e32 v11, v11, v31
	v_add_f32_e32 v12, v12, v32
	v_add_f32_e32 v13, v13, v33
	s_waitcnt vmcnt(10)
	v_add_f32_e32 v10, v10, v34
	v_add_f32_e32 v11, v11, v35
	v_add_f32_e32 v12, v12, v36
	v_add_f32_e32 v13, v13, v37
	s_waitcnt vmcnt(9)
	v_add_f32_e32 v10, v10, v38
	v_add_f32_e32 v11, v11, v39
	v_add_f32_e32 v12, v12, v40
	v_add_f32_e32 v13, v13, v41
	s_waitcnt vmcnt(8)
	v_add_f32_e32 v10, v10, v42
	v_add_f32_e32 v11, v11, v43
	v_add_f32_e32 v12, v12, v44
	v_add_f32_e32 v13, v13, v45
	s_waitcnt vmcnt(7)
	v_add_f32_e32 v10, v10, v46
	v_add_f32_e32 v11, v11, v47
	v_add_f32_e32 v12, v12, v48
	v_add_f32_e32 v13, v13, v49
	s_waitcnt vmcnt(6)
	v_add_f32_e32 v10, v10, v50
	v_add_f32_e32 v11, v11, v51
	v_add_f32_e32 v12, v12, v52
	v_add_f32_e32 v13, v13, v53
	s_waitcnt vmcnt(5)
	v_add_f32_e32 v10, v10, v54
	v_add_f32_e32 v11, v11, v55
	v_add_f32_e32 v12, v12, v56
	v_add_f32_e32 v13, v13, v57
	s_waitcnt vmcnt(4)
	v_add_f32_e32 v10, v10, v58
	v_add_f32_e32 v11, v11, v59
	v_add_f32_e32 v12, v12, v60
	v_add_f32_e32 v13, v13, v61
	s_waitcnt vmcnt(3)
	v_add_f32_e32 v10, v10, v62
	v_add_f32_e32 v11, v11, v63
	v_add_f32_e32 v12, v12, v64
	v_add_f32_e32 v13, v13, v65
	s_waitcnt vmcnt(2)
	v_add_f32_e32 v10, v10, v66
	v_add_f32_e32 v11, v11, v67
	v_add_f32_e32 v12, v12, v68
	v_add_f32_e32 v13, v13, v69
	s_waitcnt vmcnt(1)
	v_add_f32_e32 v10, v10, v70
	v_add_f32_e32 v11, v11, v71
	v_add_f32_e32 v12, v12, v72
	v_add_f32_e32 v13, v13, v73
	s_waitcnt vmcnt(0)
	v_add_f32_e32 v10, v10, v74
	v_add_f32_e32 v11, v11, v75
	v_add_f32_e32 v12, v12, v76
	v_add_f32_e32 v13, v13, v77
	ds_write_b128 v5, v[10:13] offset:4096
	s_movk_i32 s0, 0xa0
	v_cmp_gt_u32_e32 vcc, s0, v0
	v_lshlrev_b32_e32 v1, 2, v0
	s_waitcnt lgkmcnt(0)
	s_barrier
	s_and_saveexec_b64 s[0:1], vcc
	s_cbranch_execz .LBB5_4
	ds_read_b32 v14, v1 offset:4096
	ds_read_b32 v15, v1 offset:4736
	ds_read_b32 v16, v1 offset:5376
	ds_read_b32 v17, v1 offset:6016
	ds_read_b32 v18, v1 offset:6656
	ds_read_b32 v19, v1 offset:7296
	ds_read_b32 v20, v1 offset:7936
	ds_read_b32 v21, v1 offset:8576
	s_waitcnt lgkmcnt(0)
	ds_read_b32 v22, v1 offset:9216
	ds_read_b32 v23, v1 offset:9856
	ds_read_b32 v24, v1 offset:10496
	ds_read_b32 v25, v1 offset:11136
	ds_read_b32 v26, v1 offset:11776
	ds_read_b32 v27, v1 offset:12416
	ds_read_b32 v28, v1 offset:13056
	ds_read_b32 v29, v1 offset:13696
	v_add_f32_e32 v2, v14, v15
	v_add_f32_e32 v2, v2, v16
	v_add_f32_e32 v2, v2, v17
	v_add_f32_e32 v2, v2, v18
	v_add_f32_e32 v2, v2, v19
	v_add_f32_e32 v2, v2, v20
	v_add_f32_e32 v2, v2, v21
	s_waitcnt lgkmcnt(0)
	v_add_f32_e32 v2, v2, v22
	v_add_f32_e32 v2, v2, v23
	v_add_f32_e32 v2, v2, v24
	v_add_f32_e32 v2, v2, v25
	v_add_f32_e32 v2, v2, v26
	v_add_f32_e32 v2, v2, v27
	v_add_f32_e32 v2, v2, v28
	v_add_f32_e32 v2, v2, v29
	v_mul_f32_e32 v2, 0x39800000, v2
	ds_write_b32 v1, v2 offset:2560

	.amdhsa_kernel _Z12final_kernelPKfPf
		.amdhsa_group_segment_fixed_size 14336
		.amdhsa_private_segment_fixed_size 0
		.amdhsa_kernarg_size 16
		.amdhsa_user_sgpr_count 2
		.amdhsa_user_sgpr_dispatch_ptr 0
		.amdhsa_user_sgpr_queue_ptr 0
		.amdhsa_user_sgpr_kernarg_segment_ptr 1
		.amdhsa_user_sgpr_dispatch_id 0
		.amdhsa_user_sgpr_kernarg_preload_length 0
		.amdhsa_user_sgpr_kernarg_preload_offset 0
		.amdhsa_user_sgpr_private_segment_size 0
		.amdhsa_uses_dynamic_stack 0
		.amdhsa_enable_private_segment 0
		.amdhsa_system_sgpr_workgroup_id_x 1
		.amdhsa_system_sgpr_workgroup_id_y 0
		.amdhsa_system_sgpr_workgroup_id_z 0
		.amdhsa_system_sgpr_workgroup_info 0
		.amdhsa_system_vgpr_workitem_id 0
		.amdhsa_next_free_vgpr 78
		.amdhsa_next_free_sgpr 10
		.amdhsa_accum_offset 80
		.amdhsa_reserve_vcc 1
		.amdhsa_float_round_mode_32 0
		.amdhsa_float_round_mode_16_64 0
		.amdhsa_float_denorm_mode_32 3
		.amdhsa_float_denorm_mode_16_64 3
		.amdhsa_dx10_clamp 1
		.amdhsa_ieee_mode 1
		.amdhsa_fp16_overflow 0
		.amdhsa_tg_split 0
		.amdhsa_exception_fp_ieee_invalid_op 0
		.amdhsa_exception_fp_denorm_src 0
		.amdhsa_exception_fp_ieee_div_zero 0
		.amdhsa_exception_fp_ieee_overflow 0
		.amdhsa_exception_fp_ieee_underflow 0
		.amdhsa_exception_fp_ieee_inexact 0
		.amdhsa_exception_int_div_zero 0
	.end_amdhsa_kernel

amdhsa.kernels:
  - .agpr_count:     16
    .args:
      - .address_space:  global
        .offset:         0
        .size:           8
        .value_kind:     global_buffer
      - .address_space:  global
        .offset:         8
        .size:           8
        .value_kind:     global_buffer
      - .address_space:  global
        .offset:         16
        .size:           8
        .value_kind:     global_buffer
      - .address_space:  global
        .offset:         24
        .size:           8
        .value_kind:     global_buffer
      - .address_space:  global
        .offset:         32
        .size:           8
        .value_kind:     global_buffer
      - .address_space:  global
        .offset:         40
        .size:           8
        .value_kind:     global_buffer
      - .address_space:  global
        .offset:         48
        .size:           8
        .value_kind:     global_buffer
      - .address_space:  global
        .offset:         56
        .size:           8
        .value_kind:     global_buffer
      - .address_space:  global
        .offset:         64
        .size:           8
        .value_kind:     global_buffer
      - .address_space:  global
        .offset:         72
        .size:           8
        .value_kind:     global_buffer
      - .address_space:  global
        .offset:         80
        .size:           8
        .value_kind:     global_buffer
      - .address_space:  global
        .offset:         88
        .size:           8
        .value_kind:     global_buffer
      - .address_space:  global
        .offset:         96
        .size:           8
        .value_kind:     global_buffer
      - .address_space:  global
        .offset:         104
        .size:           8
        .value_kind:     global_buffer
      - .address_space:  global
        .offset:         112
        .size:           8
        .value_kind:     global_buffer
      - .address_space:  global
        .offset:         120
        .size:           8
        .value_kind:     global_buffer
      - .address_space:  global
        .offset:         128
        .size:           8
        .value_kind:     global_buffer
      - .address_space:  global
        .offset:         136
        .size:           8
        .value_kind:     global_buffer
      - .address_space:  global
        .offset:         144
        .size:           8
        .value_kind:     global_buffer
      - .address_space:  global
        .offset:         152
        .size:           8
        .value_kind:     global_buffer
    .group_segment_fixed_size: 0
    .kernarg_segment_align: 8
    .kernarg_segment_size: 160
    .language:       OpenCL C
    .language_version:
      - 2
      - 0
    .max_flat_workgroup_size: 256
    .name:           _Z11lstm_kernelPKDF16_PKDv8_DF16_S3_S3_PKfS5_S5_S5_PDF16_S6_PfS5_PS1_PK15HIP_vector_typeIfLj4EES5_S5_S7_S5_S5_S5_
    .private_segment_fixed_size: 0
    .sgpr_count:     70
    .sgpr_spill_count: 0
    .symbol:         _Z11lstm_kernelPKDF16_PKDv8_DF16_S3_S3_PKfS5_S5_S5_PDF16_S6_PfS5_PS1_PK15HIP_vector_typeIfLj4EES5_S5_S7_S5_S5_S5_.kd
    .uniform_work_group_size: 1
    .uses_dynamic_stack: false
    .vgpr_count:     228
    .vgpr_spill_count: 0
    .wavefront_size: 64
  - .agpr_count:     0
    .args:
      - .actual_access:  read_only
        .address_space:  global
        .offset:         0
        .size:           8
        .value_kind:     global_buffer
      - .actual_access:  read_only
        .address_space:  global
        .offset:         8
        .size:           8
        .value_kind:     global_buffer
      - .actual_access:  read_only
        .address_space:  global
        .offset:         16
        .size:           8
        .value_kind:     global_buffer
      - .actual_access:  write_only
        .address_space:  global
        .offset:         24
        .size:           8
        .value_kind:     global_buffer
    .group_segment_fixed_size: 0
    .kernarg_segment_align: 8
    .kernarg_segment_size: 32
    .language:       OpenCL C
    .language_version:
      - 2
      - 0
    .max_flat_workgroup_size: 256
    .name:           _Z12conv1_kernelPKfS0_S0_PDF16_
    .private_segment_fixed_size: 0
    .sgpr_count:     66
    .sgpr_spill_count: 0
    .symbol:         _Z12conv1_kernelPKfS0_S0_PDF16_.kd
    .uniform_work_group_size: 1
    .uses_dynamic_stack: false
    .vgpr_count:     59
    .vgpr_spill_count: 0
    .wavefront_size: 64
  - .agpr_count:     0
    .args:
      - .address_space:  global
        .offset:         0
        .size:           8
        .value_kind:     global_buffer
      - .address_space:  global
        .offset:         8
        .size:           8
        .value_kind:     global_buffer
      - .address_space:  global
        .offset:         16
        .size:           8
        .value_kind:     global_buffer
      - .address_space:  global
        .offset:         24
        .size:           8
        .value_kind:     global_buffer
      - .address_space:  global
        .offset:         32
        .size:           8
        .value_kind:     global_buffer
      - .address_space:  global
        .offset:         40
        .size:           8
        .value_kind:     global_buffer
      - .address_space:  global
        .offset:         48
        .size:           8
        .value_kind:     global_buffer
      - .address_space:  global
        .offset:         56
        .size:           8
        .value_kind:     global_buffer
      - .address_space:  global
        .offset:         64
        .size:           8
        .value_kind:     global_buffer
      - .address_space:  global
        .offset:         72
        .size:           8
        .value_kind:     global_buffer
      - .address_space:  global
        .offset:         80
        .size:           8
        .value_kind:     global_buffer
    .group_segment_fixed_size: 0
    .kernarg_segment_align: 8
    .kernarg_segment_size: 88
    .language:       OpenCL C
    .language_version:
      - 2
      - 0
    .max_flat_workgroup_size: 256
    .name:           _Z11prep_kernelPKfS0_S0_S0_PDv8_DF16_S2_S2_PKiS0_S2_PDv4_j
    .private_segment_fixed_size: 0
    .sgpr_count:     34
    .sgpr_spill_count: 0
    .symbol:         _Z11prep_kernelPKfS0_S0_S0_PDv8_DF16_S2_S2_PKiS0_S2_PDv4_j.kd
    .uniform_work_group_size: 1
    .uses_dynamic_stack: false
    .vgpr_count:     17
    .vgpr_spill_count: 0
    .wavefront_size: 64
  - .agpr_count:     104
    .args:
      - .address_space:  global
        .offset:         0
        .size:           8
        .value_kind:     global_buffer
      - .address_space:  global
        .offset:         8
        .size:           8
        .value_kind:     global_buffer
      - .address_space:  global
        .offset:         16
        .size:           8
        .value_kind:     global_buffer
      - .address_space:  global
        .offset:         24
        .size:           8
        .value_kind:     global_buffer
      - .address_space:  global
        .offset:         32
        .size:           8
        .value_kind:     global_buffer
    .group_segment_fixed_size: 129152
    .kernarg_segment_align: 8
    .kernarg_segment_size: 40
    .language:       OpenCL C
    .language_version:
      - 2
      - 0
    .max_flat_workgroup_size: 256
    .name:           _Z13pconv2_kernelPKDF16_PKDv8_DF16_PKfPfS6_
    .private_segment_fixed_size: 0
    .sgpr_count:     30
    .sgpr_spill_count: 0
    .symbol:         _Z13pconv2_kernelPKDF16_PKDv8_DF16_PKfPfS6_.kd
    .uniform_work_group_size: 1
    .uses_dynamic_stack: false
    .vgpr_count:     324
    .vgpr_spill_count: 0
    .wavefront_size: 64
  - .agpr_count:     40
    .args:
      - .address_space:  global
        .offset:         0
        .size:           8
        .value_kind:     global_buffer
      - .address_space:  global
        .offset:         8
        .size:           8
        .value_kind:     global_buffer
      - .address_space:  global
        .offset:         16
        .size:           8
        .value_kind:     global_buffer
      - .address_space:  global
        .offset:         24
        .size:           8
        .value_kind:     global_buffer
    .group_segment_fixed_size: 41472
    .kernarg_segment_align: 8
    .kernarg_segment_size: 32
    .language:       OpenCL C
    .language_version:
      - 2
      - 0
    .max_flat_workgroup_size: 256
    .name:           _Z11dcap_kernelPKfS0_S0_Pf
    .private_segment_fixed_size: 0
    .sgpr_count:     25
    .sgpr_spill_count: 0
    .symbol:         _Z11dcap_kernelPKfS0_S0_Pf.kd
    .uniform_work_group_size: 1
    .uses_dynamic_stack: false
    .vgpr_count:     244
    .vgpr_spill_count: 0
    .wavefront_size: 64
  - .agpr_count:     0
    .args:
      - .address_space:  global
        .offset:         0
        .size:           8
        .value_kind:     global_buffer
      - .address_space:  global
        .offset:         8
        .size:           8
        .value_kind:     global_buffer
    .group_segment_fixed_size: 14336
    .kernarg_segment_align: 8
    .kernarg_segment_size: 16
    .language:       OpenCL C
    .language_version:
      - 2
      - 0
    .max_flat_workgroup_size: 640
    .name:           _Z12final_kernelPKfPf
    .private_segment_fixed_size: 0
    .sgpr_count:     16
    .sgpr_spill_count: 0
    .symbol:         _Z12final_kernelPKfPf.kd
    .uniform_work_group_size: 1
    .uses_dynamic_stack: false
    .vgpr_count:     78
    .vgpr_spill_count: 0
    .wavefront_size: 64
